# speedup vs baseline: 1.0238x; 1.0071x over previous
_Z8k2_fusedPKDF16_PKDv8_DF16_PKfS5_S5_PfPiS6_:
	s_lshl_b32 s3, s2, 2
	s_ashr_i32 s16, s2, 4
	s_and_b32 s12, s3, 48
	s_lshl_b32 s2, s2, 4
	s_and_b32 s13, s2, 48
	s_add_i32 s2, s12, -2
	v_mul_u32_u24_e32 v1, 0x334, v0
	s_movk_i32 s15, 0xffec
	s_add_i32 s3, s13, -2
	v_lshrrev_b32_e32 v84, 2, v0
	v_mul_i32_i24_sdwa v2, v1, s15 dst_sel:DWORD dst_unused:UNUSED_PAD src0_sel:WORD_1 src1_sel:DWORD
	v_add_u32_sdwa v48, s2, v1 dst_sel:DWORD dst_unused:UNUSED_PAD src0_sel:DWORD src1_sel:WORD_1
	s_load_dwordx8 s[4:11], s[0:1], 0x0
	s_load_dwordx4 s[32:35], s[0:1], 0x20
	s_load_dwordx2 s[36:37], s[0:1], 0x38
	v_add3_u32 v49, s3, v84, v2
	v_max_i32_e32 v1, 0, v48
	s_lshl_b32 s14, s16, 12
	v_med3_i32 v2, v49, 0, 63
	v_lshlrev_b32_e32 v1, 6, v1
	v_or3_b32 v1, v1, v2, s14
	v_lshlrev_b32_e32 v2, 5, v1
	v_ashrrev_i32_e32 v3, 31, v2
	v_lshlrev_b32_e32 v85, 4, v0
	s_waitcnt lgkmcnt(0)
	v_lshl_add_u64 v[2:3], v[2:3], 1, s[4:5]
	v_and_b32_e32 v46, 48, v85
	v_mov_b32_e32 v47, 0
	v_or_b32_e32 v54, 0x200, v0
	v_lshl_add_u64 v[2:3], v[2:3], 0, v[46:47]
	v_mul_u32_u24_e32 v1, 0x334, v54
	global_load_dwordx4 v[18:21], v[2:3], off
	v_lshrrev_b32_e32 v86, 2, v54
	v_mul_i32_i24_sdwa v2, v1, s15 dst_sel:DWORD dst_unused:UNUSED_PAD src0_sel:WORD_1 src1_sel:DWORD
	v_add_u32_sdwa v50, s2, v1 dst_sel:DWORD dst_unused:UNUSED_PAD src0_sel:DWORD src1_sel:WORD_1
	v_add3_u32 v51, s3, v86, v2
	v_min_u32_e32 v1, 63, v50
	v_med3_i32 v2, v51, 0, 63
	v_lshlrev_b32_e32 v1, 6, v1
	v_or3_b32 v1, v1, v2, s14
	v_lshlrev_b32_e32 v2, 5, v1
	v_or_b32_e32 v58, 0x400, v0
	v_ashrrev_i32_e32 v3, 31, v2
	v_lshlrev_b32_e32 v87, 4, v54
	v_mul_u32_u24_e32 v1, 0x667, v58
	v_lshl_add_u64 v[2:3], v[2:3], 1, s[4:5]
	v_and_b32_e32 v4, 48, v87
	v_mov_b32_e32 v5, v47
	v_lshrrev_b32_e32 v1, 17, v1
	v_lshl_add_u64 v[2:3], v[2:3], 0, v[4:5]
	v_mul_i32_i24_e32 v4, 0xffffffec, v1
	v_add_u32_e32 v52, s2, v1
	v_lshrrev_b32_e32 v88, 2, v58
	v_add3_u32 v53, s3, v88, v4
	v_min_u32_e32 v1, 63, v52
	v_med3_i32 v4, v53, 0, 63
	v_lshlrev_b32_e32 v1, 6, v1
	v_or3_b32 v1, v1, v4, s14
	v_lshlrev_b32_e32 v4, 5, v1
	v_ashrrev_i32_e32 v5, 31, v4
	v_or_b32_e32 v89, 0x600, v0
	v_lshl_add_u64 v[4:5], v[4:5], 1, s[4:5]
	v_min_u32_e32 v1, 0x63f, v89
	v_lshl_add_u64 v[4:5], v[4:5], 0, v[46:47]
	global_load_dwordx4 v[22:25], v[2:3], off
	global_load_dwordx4 v[26:29], v[4:5], off
	v_lshrrev_b32_e32 v2, 2, v1
	v_add_u32_e32 v2, s3, v2
	s_add_i32 s15, s12, 17
	v_add_u32_e32 v55, 0xfffffe84, v2
	s_min_u32 s2, s15, 63
	v_min_u32_e32 v2, 63, v55
	v_lshl_or_b32 v2, s2, 6, v2
	v_or_b32_e32 v2, s14, v2
	v_lshlrev_b32_e32 v2, 5, v2
	v_ashrrev_i32_e32 v3, 31, v2
	v_lshlrev_b32_e32 v1, 4, v1
	v_lshl_add_u64 v[2:3], v[2:3], 1, s[4:5]
	v_and_b32_e32 v4, 48, v1
	v_mov_b32_e32 v5, v47
	v_min_u32_e32 v1, 0x47f, v58
	v_lshrrev_b32_e32 v164, 1, v0
	v_lshl_add_u64 v[2:3], v[2:3], 0, v[4:5]
	v_lshlrev_b32_e32 v90, 4, v1
	v_and_b32_e32 v162, 16, v164
	global_load_dwordx4 v[30:33], v[2:3], off
	global_load_dwordx4 v[34:37], v85, s[6:7]
	global_load_dwordx4 v[38:41], v87, s[6:7]
	global_load_dwordx4 v[42:45], v90, s[6:7]
	s_nop 0
	global_load_dwordx4 v[2:5], v162, s[8:9]
	global_load_dwordx4 v[6:9], v162, s[8:9] offset:32
	global_load_dwordx4 v[10:13], v162, s[8:9] offset:64
	global_load_dwordx4 v[14:17], v162, s[8:9] offset:96
	v_or_b32_e32 v48, v48, v49
	v_cmp_gt_u32_e32 vcc, 64, v48
	v_or_b32_e32 v48, v50, v51
	v_cmp_gt_u32_e64 s[2:3], 64, v48
	v_or_b32_e32 v48, v52, v53
	v_and_b32_e32 v1, 63, v0
	v_and_b32_e32 v165, 31, v0
	v_cmp_gt_u32_e64 s[4:5], 64, v48
	v_or_b32_e32 v48, s15, v55
	v_lshrrev_b32_e32 v163, 6, v0
	v_cmp_gt_u32_e64 s[6:7], 64, v48
	s_lshr_b32 s8, s12, 1
	s_lshr_b32 s26, s13, 1
	v_add_u32_e32 v48, s8, v163
	v_bfe_u32 v49, v0, 1, 3
	v_add_u32_e32 v49, s26, v49
	v_lshlrev_b32_e32 v48, 10, v48
	v_lshl_or_b32 v48, v49, 5, v48
	v_bfe_u32 v49, v0, 5, 1
	v_lshl_or_b32 v48, v49, 2, v48
	v_bfe_u32 v49, v0, 4, 1
	v_lshl_or_b32 v48, v49, 1, v48
	v_and_b32_e32 v49, 1, v0
	v_or_b32_e32 v48, v48, v49
	v_mul_u32_u24_e32 v59, 40, v48
	global_load_dwordx4 v[66:69], v59, s[10:11]
	global_load_dwordx4 v[50:53], v59, s[10:11] offset:16
	global_load_dwordx2 v[156:157], v59, s[10:11] offset:32
	global_load_dwordx4 v[70:73], v59, s[10:11] offset:320
	global_load_dwordx4 v[54:57], v59, s[10:11] offset:336
	global_load_dwordx2 v[154:155], v59, s[10:11] offset:352
	global_load_dwordx4 v[74:77], v59, s[10:11] offset:640
	global_load_dwordx4 v[58:61], v59, s[10:11] offset:656
	global_load_dwordx2 v[160:161], v59, s[10:11] offset:672
	global_load_dwordx4 v[78:81], v59, s[10:11] offset:960
	global_load_dwordx4 v[62:65], v59, s[10:11] offset:976
	global_load_dwordx2 v[158:159], v59, s[10:11] offset:992
	s_movk_i32 s8, 0x50
	s_waitcnt vmcnt(22)
	v_cndmask_b32_e32 v19, 0, v19, vcc
	v_cndmask_b32_e32 v18, 0, v18, vcc
	v_cndmask_b32_e32 v21, 0, v21, vcc
	v_cndmask_b32_e32 v20, 0, v20, vcc
	v_mad_u32_u24 v47, v84, s8, v46
	ds_write_b128 v47, v[18:21]
	s_waitcnt vmcnt(21)
	v_cndmask_b32_e64 v19, 0, v23, s[2:3]
	v_cndmask_b32_e64 v18, 0, v22, s[2:3]
	v_cndmask_b32_e64 v21, 0, v25, s[2:3]
	v_cndmask_b32_e64 v20, 0, v24, s[2:3]
	v_mad_u32_u24 v22, v86, s8, v46
	ds_write_b128 v22, v[18:21]
	s_waitcnt vmcnt(20)
	v_cndmask_b32_e64 v19, 0, v27, s[4:5]
	v_cndmask_b32_e64 v18, 0, v26, s[4:5]
	v_cndmask_b32_e64 v21, 0, v29, s[4:5]
	v_cndmask_b32_e64 v20, 0, v28, s[4:5]
	v_mad_u32_u24 v22, v88, s8, v46
	ds_write_b128 v22, v[18:21]
	v_lshrrev_b32_e32 v22, 2, v89
	s_waitcnt vmcnt(19)
	v_cndmask_b32_e64 v19, 0, v31, s[6:7]
	v_cndmask_b32_e64 v18, 0, v30, s[6:7]
	v_cndmask_b32_e64 v21, 0, v33, s[6:7]
	v_cndmask_b32_e64 v20, 0, v32, s[6:7]
	v_mad_u32_u24 v22, v22, s8, v46
	ds_write_b128 v22, v[18:21]
	s_waitcnt vmcnt(18)
	ds_write_b128 v85, v[34:37] offset:57920
	s_waitcnt vmcnt(17)
	ds_write_b128 v87, v[38:41] offset:57920
	s_waitcnt vmcnt(16)
	ds_write_b128 v90, v[42:45] offset:57920
	v_lshlrev_b32_e32 v18, 4, v1
	s_waitcnt lgkmcnt(0)
	s_barrier
	v_add_u32_e32 v19, 0xe240, v18
	ds_read_b128 v[150:153], v18 offset:57920
	ds_read_b128 v[146:149], v18 offset:58944
	ds_read_b128 v[142:145], v18 offset:59968
	ds_read_b128 v[138:141], v18 offset:60992
	ds_read_b128 v[134:137], v18 offset:62016
	ds_read_b128 v[130:133], v18 offset:63040
	ds_read_b128 v[126:129], v18 offset:64064
	ds_read_b128 v[122:125], v18 offset:65088
	ds_read_b128 v[118:121], v19 offset:8192
	ds_read_b128 v[114:117], v19 offset:9216
	ds_read_b128 v[110:113], v19 offset:10240
	ds_read_b128 v[106:109], v19 offset:11264
	ds_read_b128 v[102:105], v19 offset:12288
	ds_read_b128 v[98:101], v19 offset:13312
	ds_read_b128 v[94:97], v19 offset:14336
	ds_read_b128 v[90:93], v19 offset:15360
	ds_read_b128 v[86:89], v19 offset:16384
	ds_read_b128 v[82:85], v19 offset:17408
	v_lshl_or_b32 v166, v163, 5, v165
	v_mul_u32_u24_e32 v18, 0xe39, v166
	v_lshrrev_b32_e32 v168, 16, v18
	s_movk_i32 s4, 0xffee
	v_mad_i32_i24 v169, v168, s4, v166
	v_min_u32_e32 v19, 0x43, v166
	v_mad_u32_u24 v18, v168, 20, v169
	v_or_b32_e32 v165, 0x100, v19
	s_movk_i32 s2, 0xc0
	v_mul_lo_u32 v18, v18, s8
	v_mul_u32_u24_e32 v19, 0xe39, v165
	v_cmp_gt_u32_e32 vcc, s2, v0
	s_movk_i32 s2, 0xbf
	v_lshrrev_b32_e32 v167, 16, v19
	v_cmp_lt_u32_e64 s[2:3], s2, v0
	v_add_u32_e32 v171, v18, v162
	s_and_saveexec_b64 s[6:7], s[2:3]
	s_xor_b64 s[2:3], exec, s[6:7]
	s_cbranch_execz .LBB1_2
	ds_read_b128 v[34:37], v171
	ds_read_b128 v[38:41], v171 offset:32
	ds_read_b128 v[42:45], v171 offset:80
	ds_read_b128 v[46:49], v171 offset:112
	ds_read_b128 v[172:175], v171 offset:160
	ds_read_b128 v[176:179], v171 offset:192
	ds_read_b128 v[180:183], v171 offset:1600
	ds_read_b128 v[184:187], v171 offset:1632
	ds_read_b128 v[188:191], v171 offset:1680
	s_waitcnt vmcnt(12) lgkmcnt(8)
	v_mfma_f32_32x32x16_f16 v[18:33], v[150:153], v[34:37], v[2:17]
	s_waitcnt lgkmcnt(7)
	v_mfma_f32_32x32x16_f16 v[18:33], v[146:149], v[38:41], v[18:33]
	ds_read_b128 v[34:37], v171 offset:1712
	s_waitcnt lgkmcnt(7)
	v_mfma_f32_32x32x16_f16 v[18:33], v[142:145], v[42:45], v[18:33]
	ds_read_b128 v[38:41], v171 offset:1760
	s_waitcnt lgkmcnt(7)
	v_mfma_f32_32x32x16_f16 v[18:33], v[138:141], v[46:49], v[18:33]
	ds_read_b128 v[42:45], v171 offset:1792
	s_waitcnt lgkmcnt(7)
	v_mfma_f32_32x32x16_f16 v[18:33], v[134:137], v[172:175], v[18:33]
	ds_read_b128 v[46:49], v171 offset:3200
	s_waitcnt lgkmcnt(7)
	v_mfma_f32_32x32x16_f16 v[18:33], v[130:133], v[176:179], v[18:33]
	ds_read_b128 v[172:175], v171 offset:3232
	s_waitcnt lgkmcnt(7)
	v_mfma_f32_32x32x16_f16 v[18:33], v[126:129], v[180:183], v[18:33]
	ds_read_b128 v[176:179], v171 offset:3280
	s_waitcnt lgkmcnt(7)
	v_mfma_f32_32x32x16_f16 v[18:33], v[122:125], v[184:187], v[18:33]
	ds_read_b128 v[180:183], v171 offset:3312
	s_waitcnt lgkmcnt(7)
	v_mfma_f32_32x32x16_f16 v[18:33], v[118:121], v[188:191], v[18:33]
	ds_read_b128 v[184:187], v171 offset:3360
	s_waitcnt lgkmcnt(7)
	v_mfma_f32_32x32x16_f16 v[18:33], v[114:117], v[34:37], v[18:33]
	ds_read_b128 v[188:191], v171 offset:3392
	s_waitcnt lgkmcnt(7)
	v_mfma_f32_32x32x16_f16 v[18:33], v[110:113], v[38:41], v[18:33]
	s_waitcnt lgkmcnt(6)
	v_mfma_f32_32x32x16_f16 v[18:33], v[106:109], v[42:45], v[18:33]
	s_waitcnt lgkmcnt(5)
	v_mfma_f32_32x32x16_f16 v[18:33], v[102:105], v[46:49], v[18:33]
	s_waitcnt lgkmcnt(4)
	v_mfma_f32_32x32x16_f16 v[18:33], v[98:101], v[172:175], v[18:33]
	s_waitcnt lgkmcnt(3)
	v_mfma_f32_32x32x16_f16 v[18:33], v[94:97], v[176:179], v[18:33]
	s_waitcnt lgkmcnt(2)
	v_mfma_f32_32x32x16_f16 v[18:33], v[90:93], v[180:183], v[18:33]
	s_waitcnt lgkmcnt(1)
	v_mfma_f32_32x32x16_f16 v[18:33], v[86:89], v[184:187], v[18:33]
	s_waitcnt lgkmcnt(0)
	v_mfma_f32_32x32x16_f16 v[18:33], v[82:85], v[188:191], v[18:33]
	v_mov_b32_e32 v49, v17
	v_mov_b32_e32 v48, v16
	v_mov_b32_e32 v47, v15
	v_mov_b32_e32 v46, v14
	v_mov_b32_e32 v45, v13
	v_mov_b32_e32 v44, v12
	v_mov_b32_e32 v43, v11
	v_mov_b32_e32 v42, v10
	v_mov_b32_e32 v41, v9
	v_mov_b32_e32 v40, v8
	v_mov_b32_e32 v39, v7
	v_mov_b32_e32 v38, v6
	v_mov_b32_e32 v37, v5
	v_mov_b32_e32 v36, v4
	v_mov_b32_e32 v35, v3
	v_mov_b32_e32 v34, v2

.LBB1_8:
	s_or_b64 exec, exec, s[2:3]
	v_bfe_u32 v18, v0, 4, 1
	v_lshl_or_b32 v18, v163, 1, v18
	v_and_b32_e32 v22, 15, v0
	v_mad_u32_u24 v18, v18, 18, v22
	s_movk_i32 s2, 0x50
	v_mad_u32_u24 v23, v18, s2, v162
	s_waitcnt lgkmcnt(0)
	s_barrier
	ds_read_b128 v[18:21], v23 offset:32000
	ds_read_b128 v[24:27], v23 offset:32032
	ds_read_b128 v[28:31], v23 offset:32080
	ds_read_b128 v[32:35], v23 offset:32112
	ds_read_b128 v[36:39], v23 offset:32160
	ds_read_b128 v[40:43], v23 offset:32192
	ds_read_b128 v[44:47], v23 offset:33440
	ds_read_b128 v[166:169], v23 offset:33472
	ds_read_b128 v[170:173], v23 offset:33520
	s_waitcnt vmcnt(12) lgkmcnt(8)
	v_mfma_f32_32x32x16_f16 v[2:17], v[150:153], v[18:21], v[2:17]
	s_waitcnt lgkmcnt(7)
	v_mfma_f32_32x32x16_f16 v[2:17], v[146:149], v[24:27], v[2:17]
	ds_read_b128 v[18:21], v23 offset:33552
	s_waitcnt lgkmcnt(7)
	v_mfma_f32_32x32x16_f16 v[2:17], v[142:145], v[28:31], v[2:17]
	ds_read_b128 v[24:27], v23 offset:33600
	s_waitcnt lgkmcnt(7)
	v_mfma_f32_32x32x16_f16 v[2:17], v[138:141], v[32:35], v[2:17]
	ds_read_b128 v[28:31], v23 offset:33632
	s_waitcnt lgkmcnt(7)
	v_mfma_f32_32x32x16_f16 v[2:17], v[134:137], v[36:39], v[2:17]
	ds_read_b128 v[32:35], v23 offset:34880
	s_waitcnt lgkmcnt(7)
	v_mfma_f32_32x32x16_f16 v[2:17], v[130:133], v[40:43], v[2:17]
	ds_read_b128 v[36:39], v23 offset:34912
	s_waitcnt lgkmcnt(7)
	v_mfma_f32_32x32x16_f16 v[2:17], v[126:129], v[44:47], v[2:17]
	ds_read_b128 v[40:43], v23 offset:34960
	s_waitcnt lgkmcnt(7)
	v_mfma_f32_32x32x16_f16 v[2:17], v[122:125], v[166:169], v[2:17]
	ds_read_b128 v[44:47], v23 offset:34992
	s_waitcnt lgkmcnt(7)
	v_mfma_f32_32x32x16_f16 v[2:17], v[118:121], v[170:173], v[2:17]
	ds_read_b128 v[122:125], v23 offset:35040
	s_waitcnt lgkmcnt(7)
	v_mfma_f32_32x32x16_f16 v[2:17], v[114:117], v[18:21], v[2:17]
	ds_read_b128 v[118:121], v23 offset:35072
	s_waitcnt lgkmcnt(7)
	v_mfma_f32_32x32x16_f16 v[2:17], v[110:113], v[24:27], v[2:17]
	s_waitcnt lgkmcnt(6)
	v_mfma_f32_32x32x16_f16 v[2:17], v[106:109], v[28:31], v[2:17]
	s_waitcnt lgkmcnt(5)
	v_mfma_f32_32x32x16_f16 v[2:17], v[102:105], v[32:35], v[2:17]
	s_waitcnt lgkmcnt(4)
	v_mfma_f32_32x32x16_f16 v[2:17], v[98:101], v[36:39], v[2:17]
	s_waitcnt lgkmcnt(3)
	v_mfma_f32_32x32x16_f16 v[2:17], v[94:97], v[40:43], v[2:17]
	s_waitcnt lgkmcnt(2)
	v_mfma_f32_32x32x16_f16 v[2:17], v[90:93], v[44:47], v[2:17]
	s_waitcnt lgkmcnt(1)
	v_mfma_f32_32x32x16_f16 v[2:17], v[86:89], v[122:125], v[2:17]
	s_waitcnt lgkmcnt(0)
	v_mfma_f32_32x32x16_f16 v[2:17], v[82:85], v[118:121], v[2:17]
	s_nop 11
	v_max_f32_dpp v2, v2, v2 quad_perm:[1,0,3,2] row_mask:0xf bank_mask:0xf
	v_max_f32_dpp v3, v3, v3 quad_perm:[1,0,3,2] row_mask:0xf bank_mask:0xf
	v_max_f32_dpp v4, v4, v4 quad_perm:[1,0,3,2] row_mask:0xf bank_mask:0xf
	v_max_f32_dpp v5, v5, v5 quad_perm:[1,0,3,2] row_mask:0xf bank_mask:0xf
	v_max_f32_dpp v6, v6, v6 quad_perm:[1,0,3,2] row_mask:0xf bank_mask:0xf
	v_max_f32_dpp v7, v7, v7 quad_perm:[1,0,3,2] row_mask:0xf bank_mask:0xf
	v_max_f32_dpp v8, v8, v8 quad_perm:[1,0,3,2] row_mask:0xf bank_mask:0xf
	v_max_f32_dpp v9, v9, v9 quad_perm:[1,0,3,2] row_mask:0xf bank_mask:0xf
	v_max_f32_dpp v10, v10, v10 quad_perm:[1,0,3,2] row_mask:0xf bank_mask:0xf
	v_max_f32_dpp v11, v11, v11 quad_perm:[1,0,3,2] row_mask:0xf bank_mask:0xf
	v_max_f32_dpp v12, v12, v12 quad_perm:[1,0,3,2] row_mask:0xf bank_mask:0xf
	v_max_f32_dpp v13, v13, v13 quad_perm:[1,0,3,2] row_mask:0xf bank_mask:0xf
	v_max_f32_dpp v14, v14, v14 quad_perm:[1,0,3,2] row_mask:0xf bank_mask:0xf
	v_max_f32_dpp v15, v15, v15 quad_perm:[1,0,3,2] row_mask:0xf bank_mask:0xf
	v_max_f32_dpp v16, v16, v16 quad_perm:[1,0,3,2] row_mask:0xf bank_mask:0xf
	v_max_f32_dpp v17, v17, v17 quad_perm:[1,0,3,2] row_mask:0xf bank_mask:0xf
	v_permlane16_swap_b32 v2, v4
	v_permlane16_swap_b32 v3, v5
	v_permlane16_swap_b32 v6, v8
	v_permlane16_swap_b32 v7, v9
	v_permlane16_swap_b32 v10, v12
	v_permlane16_swap_b32 v11, v13
	v_permlane16_swap_b32 v14, v16
	v_permlane16_swap_b32 v15, v17
	v_and_b32_e32 v18, 1, v0
	v_cmp_eq_u32_e32 vcc, 1, v18
	v_max3_f32 v2, v2, v4, 0
	v_max3_f32 v3, v3, v5, 0
	v_max3_f32 v6, v6, v8, 0
	v_max3_f32 v7, v7, v9, 0
	v_max3_f32 v10, v10, v12, 0
	v_max3_f32 v11, v11, v13, 0
	v_max3_f32 v14, v14, v16, 0
	v_max3_f32 v15, v15, v17, 0
	v_cndmask_b32_e32 v20, v2, v3, vcc
	v_cndmask_b32_e32 v22, v6, v7, vcc
	v_cndmask_b32_e32 v24, v10, v11, vcc
	v_cndmask_b32_e32 v26, v14, v15, vcc
	s_waitcnt vmcnt(0)
	v_pk_fma_f32 v[2:3], v[20:21], v[66:67], 0 op_sel_hi:[0,1,0]
	v_pk_fma_f32 v[6:7], v[20:21], v[68:69], 0 op_sel_hi:[0,1,0]
	v_pk_fma_f32 v[10:11], v[20:21], v[50:51], 0 op_sel_hi:[0,1,0]
	v_pk_fma_f32 v[14:15], v[20:21], v[52:53], 0 op_sel_hi:[0,1,0]
	v_pk_fma_f32 v[18:19], v[20:21], v[156:157], 0 op_sel_hi:[0,1,0]
	v_pk_fma_f32 v[2:3], v[22:23], v[70:71], v[2:3] op_sel_hi:[0,1,1]
	v_pk_fma_f32 v[6:7], v[22:23], v[72:73], v[6:7] op_sel_hi:[0,1,1]
	v_pk_fma_f32 v[10:11], v[22:23], v[54:55], v[10:11] op_sel_hi:[0,1,1]
	v_pk_fma_f32 v[14:15], v[22:23], v[56:57], v[14:15] op_sel_hi:[0,1,1]
	v_pk_fma_f32 v[18:19], v[22:23], v[154:155], v[18:19] op_sel_hi:[0,1,1]
	v_pk_fma_f32 v[2:3], v[24:25], v[74:75], v[2:3] op_sel_hi:[0,1,1]
	v_pk_fma_f32 v[6:7], v[24:25], v[76:77], v[6:7] op_sel_hi:[0,1,1]
	v_pk_fma_f32 v[10:11], v[24:25], v[58:59], v[10:11] op_sel_hi:[0,1,1]
	v_pk_fma_f32 v[14:15], v[24:25], v[60:61], v[14:15] op_sel_hi:[0,1,1]
	v_pk_fma_f32 v[18:19], v[24:25], v[160:161], v[18:19] op_sel_hi:[0,1,1]
	v_pk_fma_f32 v[2:3], v[26:27], v[78:79], v[2:3] op_sel_hi:[0,1,1]
	v_pk_fma_f32 v[6:7], v[26:27], v[80:81], v[6:7] op_sel_hi:[0,1,1]
	v_pk_fma_f32 v[10:11], v[26:27], v[62:63], v[10:11] op_sel_hi:[0,1,1]
	v_pk_fma_f32 v[14:15], v[26:27], v[64:65], v[14:15] op_sel_hi:[0,1,1]
	v_pk_fma_f32 v[18:19], v[26:27], v[158:159], v[18:19] op_sel_hi:[0,1,1]
	v_and_b32_e32 v28, 15, v0
	v_cmp_eq_u32_e32 vcc, 15, v28
	v_add_f32_dpp v2, v2, v2 row_shr:1 row_mask:0xf bank_mask:0xf bound_ctrl:1
	v_add_f32_dpp v3, v3, v3 row_shr:1 row_mask:0xf bank_mask:0xf bound_ctrl:1
	v_add_f32_dpp v6, v6, v6 row_shr:1 row_mask:0xf bank_mask:0xf bound_ctrl:1
	v_add_f32_dpp v7, v7, v7 row_shr:1 row_mask:0xf bank_mask:0xf bound_ctrl:1
	v_add_f32_dpp v10, v10, v10 row_shr:1 row_mask:0xf bank_mask:0xf bound_ctrl:1
	v_add_f32_dpp v11, v11, v11 row_shr:1 row_mask:0xf bank_mask:0xf bound_ctrl:1
	v_add_f32_dpp v14, v14, v14 row_shr:1 row_mask:0xf bank_mask:0xf bound_ctrl:1
	v_add_f32_dpp v15, v15, v15 row_shr:1 row_mask:0xf bank_mask:0xf bound_ctrl:1
	v_add_f32_dpp v18, v18, v18 row_shr:1 row_mask:0xf bank_mask:0xf bound_ctrl:1
	v_add_f32_dpp v19, v19, v19 row_shr:1 row_mask:0xf bank_mask:0xf bound_ctrl:1
	v_add_f32_dpp v2, v2, v2 row_shr:2 row_mask:0xf bank_mask:0xf bound_ctrl:1
	v_add_f32_dpp v3, v3, v3 row_shr:2 row_mask:0xf bank_mask:0xf bound_ctrl:1
	v_add_f32_dpp v6, v6, v6 row_shr:2 row_mask:0xf bank_mask:0xf bound_ctrl:1
	v_add_f32_dpp v7, v7, v7 row_shr:2 row_mask:0xf bank_mask:0xf bound_ctrl:1
	v_add_f32_dpp v10, v10, v10 row_shr:2 row_mask:0xf bank_mask:0xf bound_ctrl:1
	v_add_f32_dpp v11, v11, v11 row_shr:2 row_mask:0xf bank_mask:0xf bound_ctrl:1
	v_add_f32_dpp v14, v14, v14 row_shr:2 row_mask:0xf bank_mask:0xf bound_ctrl:1
	v_add_f32_dpp v15, v15, v15 row_shr:2 row_mask:0xf bank_mask:0xf bound_ctrl:1
	v_add_f32_dpp v18, v18, v18 row_shr:2 row_mask:0xf bank_mask:0xf bound_ctrl:1
	v_add_f32_dpp v19, v19, v19 row_shr:2 row_mask:0xf bank_mask:0xf bound_ctrl:1
	v_add_f32_dpp v2, v2, v2 row_shr:4 row_mask:0xf bank_mask:0xf bound_ctrl:1
	v_add_f32_dpp v3, v3, v3 row_shr:4 row_mask:0xf bank_mask:0xf bound_ctrl:1
	v_add_f32_dpp v6, v6, v6 row_shr:4 row_mask:0xf bank_mask:0xf bound_ctrl:1
	v_add_f32_dpp v7, v7, v7 row_shr:4 row_mask:0xf bank_mask:0xf bound_ctrl:1
	v_add_f32_dpp v10, v10, v10 row_shr:4 row_mask:0xf bank_mask:0xf bound_ctrl:1
	v_add_f32_dpp v11, v11, v11 row_shr:4 row_mask:0xf bank_mask:0xf bound_ctrl:1
	v_add_f32_dpp v14, v14, v14 row_shr:4 row_mask:0xf bank_mask:0xf bound_ctrl:1
	v_add_f32_dpp v15, v15, v15 row_shr:4 row_mask:0xf bank_mask:0xf bound_ctrl:1
	v_add_f32_dpp v18, v18, v18 row_shr:4 row_mask:0xf bank_mask:0xf bound_ctrl:1
	v_add_f32_dpp v19, v19, v19 row_shr:4 row_mask:0xf bank_mask:0xf bound_ctrl:1
	v_add_f32_dpp v2, v2, v2 row_shr:8 row_mask:0xf bank_mask:0xf bound_ctrl:1
	v_add_f32_dpp v3, v3, v3 row_shr:8 row_mask:0xf bank_mask:0xf bound_ctrl:1
	v_add_f32_dpp v6, v6, v6 row_shr:8 row_mask:0xf bank_mask:0xf bound_ctrl:1
	v_add_f32_dpp v7, v7, v7 row_shr:8 row_mask:0xf bank_mask:0xf bound_ctrl:1
	v_add_f32_dpp v10, v10, v10 row_shr:8 row_mask:0xf bank_mask:0xf bound_ctrl:1
	v_add_f32_dpp v11, v11, v11 row_shr:8 row_mask:0xf bank_mask:0xf bound_ctrl:1
	v_add_f32_dpp v14, v14, v14 row_shr:8 row_mask:0xf bank_mask:0xf bound_ctrl:1
	v_add_f32_dpp v15, v15, v15 row_shr:8 row_mask:0xf bank_mask:0xf bound_ctrl:1
	v_add_f32_dpp v18, v18, v18 row_shr:8 row_mask:0xf bank_mask:0xf bound_ctrl:1
	v_add_f32_dpp v19, v19, v19 row_shr:8 row_mask:0xf bank_mask:0xf bound_ctrl:1
	s_and_saveexec_b64 s[2:3], vcc
	s_cbranch_execz .LBB1_12
	v_lshrrev_b32_e32 v1, 4, v1
	v_mul_u32_u24_e32 v22, 0xa0, v163
	v_mul_u32_u24_e32 v1, 40, v1
	s_mov_b32 s4, 0x14a40
	v_add3_u32 v1, v22, v1, s4
	ds_write2_b64 v1, v[2:3], v[6:7] offset1:1
	ds_write2_b64 v1, v[10:11], v[14:15] offset0:2 offset1:3
	ds_write_b64 v1, v[18:19] offset:32
